# baseline (speedup 1.0000x reference)
_Z9ssim_mainPKfS0_S0_Pf:
	v_readfirstlane_b32 s29, v0
	s_load_dwordx4 s[4:7], s[0:1], 0x0
	s_load_dwordx4 s[8:11], s[0:1], 0x10
	s_mov_b32 s51, 0x44800000
	s_mov_b32 s38, 0
	s_mov_b32 s39, -1
	s_lshr_b32 s12, s29, 6
	s_and_b32 s13, s2, 7
	s_lshl_b32 s13, s13, 5
	s_lshr_b32 s14, s2, 3
	s_add_u32 s13, s13, s14
	s_lshr_b32 s14, s13, 3
	s_and_b32 s15, s13, 7
	s_lshl_b32 s16, s14, 20
	s_lshl_b32 s17, s15, 17
	s_add_u32 s16, s16, s17
	s_lshl_b32 s17, s12, 8
	s_add_u32 s16, s16, s17
	s_lshl_b32 s27, s12, 2
	s_add_u32 s27, s27, 0x10000
	v_and_b32_e32 v8, 63, v0
	v_and_b32_e32 v169, 15, v0
	v_bfe_u32 v164, v0, 4, 2
	v_mov_b32_e32 v6, s27
	v_mov_b32_e32 v168, 0
	ds_write_b32 v6, v168 offset:0
	ds_write_b32 v6, v168 offset:32
	ds_write_b32 v6, v168 offset:64
	ds_write_b32 v6, v168 offset:96
	v_lshrrev_b32_e32 v167, 2, v169
	v_lshlrev_b32_e32 v167, 5, v167
	v_and_b32_e32 v168, 1, v169
	v_lshl_or_b32 v167, v168, 4, v167
	v_bfe_u32 v168, v169, 1, 1
	v_lshl_or_b32 v167, v168, 7, v167
	v_lshl_or_b32 v9, v164, 14, v167
	v_and_b32_e32 v168, 1, v164
	v_lshl_or_b32 v23, v168, 14, v167
	v_lshrrev_b32_e32 v168, 1, v164
	v_lshl_or_b32 v23, v168, 13, v23
	v_add_u32_e32 v237, 0x1000, v9
	v_add_u32_e32 v238, 0x2000, v9
	v_add_u32_e32 v239, 0x3000, v9
	v_add_u32_e32 v240, 0x10000, v9
	v_add_u32_e32 v241, 0x11000, v9
	v_add_u32_e32 v242, 0x12000, v9
	v_add_u32_e32 v243, 0x13000, v9
	v_lshlrev_b32_e32 v167, 3, v164
	v_xor_b32_e32 v168, 16, v167
	v_sub_u32_e32 v165, v167, v169
	v_sub_u32_e32 v166, v168, v169
	v_add_u32_e32 v172, 0, v165
	v_min_u32_e32 v172, 11, v172
	v_lshlrev_b32_e32 v172, 2, v172
	v_add_u32_e32 v173, 1, v165
	v_min_u32_e32 v173, 11, v173
	v_lshlrev_b32_e32 v173, 2, v173
	v_add_u32_e32 v174, 2, v165
	v_min_u32_e32 v174, 11, v174
	v_lshlrev_b32_e32 v174, 2, v174
	v_add_u32_e32 v175, 3, v165
	v_min_u32_e32 v175, 11, v175
	v_lshlrev_b32_e32 v175, 2, v175
	v_add_u32_e32 v176, 4, v165
	v_min_u32_e32 v176, 11, v176
	v_lshlrev_b32_e32 v176, 2, v176
	v_add_u32_e32 v177, 5, v165
	v_min_u32_e32 v177, 11, v177
	v_lshlrev_b32_e32 v177, 2, v177
	v_add_u32_e32 v178, 6, v165
	v_min_u32_e32 v178, 11, v178
	v_lshlrev_b32_e32 v178, 2, v178
	v_add_u32_e32 v179, 7, v165
	v_min_u32_e32 v179, 11, v179
	v_lshlrev_b32_e32 v179, 2, v179
	v_add_u32_e32 v180, 0, v166
	v_min_u32_e32 v180, 11, v180
	v_lshlrev_b32_e32 v180, 2, v180
	v_add_u32_e32 v181, 1, v166
	v_min_u32_e32 v181, 11, v181
	v_lshlrev_b32_e32 v181, 2, v181
	v_add_u32_e32 v182, 2, v166
	v_min_u32_e32 v182, 11, v182
	v_lshlrev_b32_e32 v182, 2, v182
	v_add_u32_e32 v183, 3, v166
	v_min_u32_e32 v183, 11, v183
	v_lshlrev_b32_e32 v183, 2, v183
	v_add_u32_e32 v184, 4, v166
	v_min_u32_e32 v184, 11, v184
	v_lshlrev_b32_e32 v184, 2, v184
	v_add_u32_e32 v185, 5, v166
	v_min_u32_e32 v185, 11, v185
	v_lshlrev_b32_e32 v185, 2, v185
	v_add_u32_e32 v186, 6, v166
	v_min_u32_e32 v186, 11, v186
	v_lshlrev_b32_e32 v186, 2, v186
	v_add_u32_e32 v187, 7, v166
	v_min_u32_e32 v187, 11, v187
	v_lshlrev_b32_e32 v187, 2, v187
	s_waitcnt lgkmcnt(0)
	s_load_dwordx8 s[40:47], s[8:9], 0x0
	s_load_dwordx2 s[48:49], s[8:9], 0x20
	s_load_dword s50, s[8:9], 0x28
	s_add_u32 s18, s4, s16
	s_addc_u32 s19, s5, 0
	s_add_u32 s20, s6, s16
	s_addc_u32 s21, s7, 0
	global_load_dwordx4 v[36:39], v9, s[18:19] offset:0 sc1 nt
	global_load_dwordx4 v[40:43], v9, s[18:19] offset:2048 sc1 nt
	global_load_dwordx4 v[68:71], v9, s[20:21] offset:0 sc1 nt
	global_load_dwordx4 v[72:75], v9, s[20:21] offset:2048 sc1 nt
	global_load_dwordx4 v[44:47], v237, s[18:19] offset:0 sc1 nt
	global_load_dwordx4 v[48:51], v237, s[18:19] offset:2048 sc1 nt
	global_load_dwordx4 v[76:79], v237, s[20:21] offset:0 sc1 nt
	global_load_dwordx4 v[80:83], v237, s[20:21] offset:2048 sc1 nt
	global_load_dwordx4 v[52:55], v238, s[18:19] offset:0 sc1 nt
	global_load_dwordx4 v[56:59], v238, s[18:19] offset:2048 sc1 nt
	global_load_dwordx4 v[84:87], v238, s[20:21] offset:0 sc1 nt
	global_load_dwordx4 v[88:91], v238, s[20:21] offset:2048 sc1 nt
	global_load_dwordx4 v[60:63], v239, s[18:19] offset:0 sc1 nt
	global_load_dwordx4 v[64:67], v239, s[18:19] offset:2048 sc1 nt
	global_load_dwordx4 v[92:95], v239, s[20:21] offset:0 sc1 nt
	global_load_dwordx4 v[96:99], v239, s[20:21] offset:2048 sc1 nt
	global_load_dwordx4 v[100:103], v240, s[18:19] offset:0 sc1 nt
	global_load_dwordx4 v[104:107], v240, s[18:19] offset:2048 sc1 nt
	global_load_dwordx4 v[132:135], v240, s[20:21] offset:0 sc1 nt
	global_load_dwordx4 v[136:139], v240, s[20:21] offset:2048 sc1 nt
	global_load_dwordx4 v[108:111], v241, s[18:19] offset:0 sc1 nt
	global_load_dwordx4 v[112:115], v241, s[18:19] offset:2048 sc1 nt
	global_load_dwordx4 v[140:143], v241, s[20:21] offset:0 sc1 nt
	global_load_dwordx4 v[144:147], v241, s[20:21] offset:2048 sc1 nt
	global_load_dwordx4 v[116:119], v242, s[18:19] offset:0 sc1 nt
	global_load_dwordx4 v[120:123], v242, s[18:19] offset:2048 sc1 nt
	global_load_dwordx4 v[148:151], v242, s[20:21] offset:0 sc1 nt
	global_load_dwordx4 v[152:155], v242, s[20:21] offset:2048 sc1 nt
	global_load_dwordx4 v[124:127], v243, s[18:19] offset:0 sc1 nt
	global_load_dwordx4 v[128:131], v243, s[18:19] offset:2048 sc1 nt
	global_load_dwordx4 v[156:159], v243, s[20:21] offset:0 sc1 nt
	global_load_dwordx4 v[160:163], v243, s[20:21] offset:2048 sc1 nt
	s_cmp_eq_u32 s15, 7
	s_cselect_b32 s22, 0, 0x20000
	s_add_u32 s84, s18, s22
	s_addc_u32 s85, s19, 0
	s_add_u32 s86, s18, s22
	s_addc_u32 s87, s19, 0
	s_add_u32 s86, s86, 0x1000
	s_addc_u32 s87, s87, 0
	s_add_u32 s88, s20, s22
	s_addc_u32 s89, s21, 0
	s_add_u32 s90, s20, s22
	s_addc_u32 s91, s21, 0
	s_add_u32 s90, s90, 0x1000
	s_addc_u32 s91, s91, 0
	s_waitcnt lgkmcnt(0)
	v_writelane_b32 v171, s40, 0
	v_writelane_b32 v171, s41, 1
	v_writelane_b32 v171, s42, 2
	v_writelane_b32 v171, s43, 3
	v_writelane_b32 v171, s44, 4
	v_writelane_b32 v171, s45, 5
	v_writelane_b32 v171, s46, 6
	v_writelane_b32 v171, s47, 7
	v_writelane_b32 v171, s48, 8
	v_writelane_b32 v171, s49, 9
	v_writelane_b32 v171, s50, 10
	v_writelane_b32 v171, 0, 11
	v_fma_mixlo_f16 v171, v171, s51, 0
	ds_bpermute_b32 v188, v172, v171
	ds_bpermute_b32 v189, v173, v171
	ds_bpermute_b32 v190, v174, v171
	ds_bpermute_b32 v191, v175, v171
	ds_bpermute_b32 v192, v176, v171
	ds_bpermute_b32 v193, v177, v171
	ds_bpermute_b32 v194, v178, v171
	ds_bpermute_b32 v195, v179, v171
	v_mov_b32_e32 v229, 0x44800000
	v_fma_mixlo_f16 v228, s40, v229, 0
	v_cvt_f32_f16_e32 v228, v228
	v_cvt_f64_f32_e32 v[212:213], v228
	v_add_f64 v[212:213], v[212:213], 0
	v_fma_mixlo_f16 v228, s41, v229, 0
	v_cvt_f32_f16_e32 v228, v228
	v_cvt_f64_f32_e32 v[214:215], v228
	v_add_f64 v[212:213], v[212:213], v[214:215]
	v_fma_mixlo_f16 v228, s42, v229, 0
	v_cvt_f32_f16_e32 v228, v228
	v_cvt_f64_f32_e32 v[214:215], v228
	v_add_f64 v[212:213], v[212:213], v[214:215]
	v_fma_mixlo_f16 v228, s43, v229, 0
	v_cvt_f32_f16_e32 v228, v228
	v_cvt_f64_f32_e32 v[214:215], v228
	v_add_f64 v[212:213], v[212:213], v[214:215]
	v_fma_mixlo_f16 v228, s44, v229, 0
	v_cvt_f32_f16_e32 v228, v228
	v_cvt_f64_f32_e32 v[214:215], v228
	v_add_f64 v[212:213], v[212:213], v[214:215]
	v_fma_mixlo_f16 v228, s45, v229, 0
	v_cvt_f32_f16_e32 v228, v228
	v_cvt_f64_f32_e32 v[214:215], v228
	v_add_f64 v[212:213], v[212:213], v[214:215]
	v_fma_mixlo_f16 v228, s46, v229, 0
	v_cvt_f32_f16_e32 v228, v228
	v_cvt_f64_f32_e32 v[214:215], v228
	v_add_f64 v[212:213], v[212:213], v[214:215]
	v_fma_mixlo_f16 v228, s47, v229, 0
	v_cvt_f32_f16_e32 v228, v228
	v_cvt_f64_f32_e32 v[214:215], v228
	v_add_f64 v[212:213], v[212:213], v[214:215]
	v_fma_mixlo_f16 v228, s48, v229, 0
	v_cvt_f32_f16_e32 v228, v228
	v_cvt_f64_f32_e32 v[214:215], v228
	v_add_f64 v[212:213], v[212:213], v[214:215]
	v_fma_mixlo_f16 v228, s49, v229, 0
	v_cvt_f32_f16_e32 v228, v228
	v_cvt_f64_f32_e32 v[214:215], v228
	v_add_f64 v[212:213], v[212:213], v[214:215]
	v_fma_mixlo_f16 v228, s50, v229, 0
	v_cvt_f32_f16_e32 v228, v228
	v_cvt_f64_f32_e32 v[214:215], v228
	v_add_f64 v[212:213], v[212:213], v[214:215]
	s_waitcnt lgkmcnt(7)
	ds_bpermute_b32 v196, v180, v171
	ds_bpermute_b32 v197, v181, v171
	ds_bpermute_b32 v198, v182, v171
	ds_bpermute_b32 v199, v183, v171
	ds_bpermute_b32 v200, v184, v171
	ds_bpermute_b32 v201, v185, v171
	ds_bpermute_b32 v202, v186, v171
	ds_bpermute_b32 v203, v187, v171
	v_mul_f64 v[212:213], v[212:213], v[212:213]
	v_mul_f64 v[216:217], v[212:213], 0.5
	v_add_f64 v[218:219], v[216:217], v[216:217]
	s_mov_b32 s36, 0xeb1c432d
	s_mov_b32 s37, 0x3f1a36e2
	v_mul_f64 v[220:221], v[212:213], s[36:37]
	v_mul_f64 v[222:223], v[216:217], v[218:219]
	v_fmac_f64_e32 v[222:223], v[212:213], v[220:221]
	v_add_f64 v[224:225], v[212:213], v[212:213]
	s_mov_b32 s36, 0x487fcb92
	s_mov_b32 s37, 0x3f4d7dbf
	v_mul_f64 v[226:227], v[212:213], s[36:37]
	v_cvt_f32_f64_e32 v0, v[226:227]
	v_mov_b32_e32 v1, v0
	v_mov_b32_e32 v2, v0
	v_mov_b32_e32 v3, v0
	v_cvt_f32_f64_e32 v10, v[218:219]
	v_cvt_f32_f64_e32 v11, v[222:223]
	v_cvt_f32_f64_e32 v12, v[212:213]
	v_cvt_f32_f64_e32 v13, v[224:225]
	v_mul_f64 v[226:227], v[212:213], v[226:227]
	v_cvt_f32_f64_e32 v14, v[226:227]
	v_lshlrev_b32_e32 v167, 2, v164
	s_cmp_eq_u32 s12, 0
	s_cselect_b32 s23, 6, 64
	v_add_u32_e32 v168, 0, v167
	v_cmp_gt_u32_e32 vcc, s23, v168
	s_nop 1
	v_cndmask_b32_e64 v15, 0, 1.0, vcc
	v_add_u32_e32 v168, 1, v167
	v_cmp_gt_u32_e32 vcc, s23, v168
	s_nop 1
	v_cndmask_b32_e64 v16, 0, 1.0, vcc
	v_add_u32_e32 v168, 2, v167
	v_cmp_gt_u32_e32 vcc, s23, v168
	s_nop 1
	v_cndmask_b32_e64 v17, 0, 1.0, vcc
	v_add_u32_e32 v168, 3, v167
	v_cmp_gt_u32_e32 vcc, s23, v168
	s_nop 1
	v_cndmask_b32_e64 v18, 0, 1.0, vcc
	v_and_b32_e32 v167, 31, v8
	v_lshlrev_b32_e32 v167, 4, v167
	s_lshl_b32 s24, s12, 11
	s_add_i32 s25, s12, 7
	s_and_b32 s25, s25, 7
	s_lshl_b32 s26, s25, 11
	v_or_b32_e32 v4, s24, v167
	v_or_b32_e32 v5, s26, v167
	s_lshl_b32 s28, s25, 2
	s_add_u32 s28, s28, 0x10000
	v_mov_b32_e32 v7, s28
	v_mov_b32_e32 v19, 0
	v_mov_b32_e32 v20, 0
	v_mov_b32_e32 v21, 0
	v_mov_b32_e32 v22, 0
	s_waitcnt lgkmcnt(0)
	v_cmp_lt_u32_e64 s[32:33], 31, v8
	v_cmp_gt_u32_e64 s[34:35], 32, v8
	v_pack_b32_f16 v24, v188, v189
	v_pack_b32_f16 v25, v190, v191
	v_pack_b32_f16 v26, v192, v193
	v_pack_b32_f16 v27, v194, v195
	v_pack_b32_f16 v167, v196, v197
	v_cndmask_b32_e64 v28, 0, v167, s[32:33]
	v_cndmask_b32_e64 v32, 0, v167, s[34:35]
	v_pack_b32_f16 v167, v198, v199
	v_cndmask_b32_e64 v29, 0, v167, s[32:33]
	v_cndmask_b32_e64 v33, 0, v167, s[34:35]
	v_pack_b32_f16 v167, v200, v201
	v_cndmask_b32_e64 v30, 0, v167, s[32:33]
	v_cndmask_b32_e64 v34, 0, v167, s[34:35]
	v_pack_b32_f16 v167, v202, v203
	v_cndmask_b32_e64 v31, 0, v167, s[32:33]
	v_cndmask_b32_e64 v35, 0, v167, s[34:35]
	s_waitcnt lgkmcnt(0)
	s_cmp_lt_u32 s12, 4
	s_cbranch_scc1 .Lq_noprio
	s_setprio 1
